# agg_ln1 gather loop hand-written (scalar row addressing and type counts, exact tail via entry points instead of per-row masking); ln2_k output stores nt
# speedup vs baseline: 1.1080x; 1.0203x over previous
_Z7agg_ln1PKDF16_S0_S0_PKiS2_S2_PKfS4_S4_PDF16_S4_S4_S5_S5_:
	s_cmpk_gt_u32 s2, 0xff
	s_mov_b64 s[4:5], -1
	s_cbranch_scc0 .LBB1_28
	v_lshl_or_b32 v1, s2, 8, v0
	v_add_u32_e32 v1, 0xffff0000, v1
	s_mov_b32 s3, 0x9c400
	v_cmp_gt_u32_e32 vcc, s3, v1
	s_and_saveexec_b64 s[18:19], vcc
	s_cbranch_execz .LBB1_27
	s_load_dwordx2 s[4:5], s[0:1], 0x20
	s_load_dwordx2 s[6:7], s[0:1], 0x18
	v_lshrrev_b32_e32 v1, 6, v1
	v_lshlrev_b32_e32 v2, 4, v1
	v_and_b32_e32 v24, 63, v0
	v_lshlrev_b32_e32 v8, 3, v24
	s_waitcnt lgkmcnt(0)
	global_load_dwordx4 v[28:31], v2, s[6:7]
	global_load_dwordx4 v[2:5], v2, s[4:5]
	s_waitcnt vmcnt(0)
	v_add_u32_e32 v26, v3, v2
	v_add_u32_e32 v3, v26, v4
	v_add_u32_e32 v25, v3, v5
	v_cmp_gt_i32_e32 vcc, 1, v25
	s_and_saveexec_b64 s[4:5], vcc
	s_xor_b64 s[4:5], exec, s[4:5]
	v_mov_b32_e32 v9, 0
	s_or_saveexec_b64 s[22:23], s[4:5]
	s_load_dwordx2 s[20:21], s[0:1], 0x48
	v_mov_b32_e32 v11, 0
	v_mov_b64_e32 v[18:19], 0
	v_mov_b32_e32 v10, v11
	v_mov_b32_e32 v13, v11
	v_mov_b32_e32 v12, v11
	v_mov_b32_e32 v15, v11
	v_mov_b32_e32 v14, v11
	v_mov_b32_e32 v17, v11
	v_mov_b32_e32 v16, v11
	s_xor_b64 exec, exec, s[22:23]
	s_cbranch_execz .LBB1_26
	s_load_dwordx2 s[24:25], s[0:1], 0x28
	s_load_dwordx2 s[26:27], s[0:1], 0x0
	v_readfirstlane_b32 s2, v25
	v_readfirstlane_b32 s4, v2
	v_readfirstlane_b32 s5, v26
	v_readfirstlane_b32 s6, v3
	v_readfirstlane_b32 s8, v28
	v_readfirstlane_b32 s9, v29
	v_readfirstlane_b32 s10, v30
	v_readfirstlane_b32 s11, v31
	v_lshrrev_b32_e32 v20, 3, v24
	v_lshlrev_b32_e32 v20, 2, v20
	v_mov_b32_e32 v9, 0
	v_mov_b32_e32 v10, 0
	v_mov_b32_e32 v11, 0
	v_mov_b32_e32 v12, 0
	v_mov_b32_e32 v13, 0
	v_mov_b32_e32 v14, 0
	v_mov_b32_e32 v15, 0
	v_mov_b32_e32 v16, 0
	v_mov_b32_e32 v17, 0
	s_sub_u32 s9, s9, s4
	s_sub_u32 s10, s10, s5
	s_sub_u32 s11, s11, s6
	s_mov_b64 s[12:13], 0
	s_mov_b32 s3, 0
	s_sub_u32 s7, s2, 1
	s_waitcnt lgkmcnt(0)
.Lagg_outer:
	v_add_u32_e32 v4, s3, v24
	v_min_u32_e32 v4, s7, v4
	v_add_u32_e32 v5, s11, v4
	v_add_u32_e32 v7, s10, v4
	v_cmp_gt_u32_e32 vcc, s6, v4
	s_nop 1
	v_cndmask_b32_e32 v5, v5, v7, vcc
	v_add_u32_e32 v7, s9, v4
	v_cmp_gt_u32_e32 vcc, s5, v4
	s_nop 1
	v_cndmask_b32_e32 v5, v5, v7, vcc
	v_add_u32_e32 v7, s8, v4
	v_cmp_gt_u32_e32 vcc, s4, v4
	s_nop 1
	v_cndmask_b32_e32 v5, v5, v7, vcc
	v_lshlrev_b32_e32 v5, 2, v5
	global_load_dword v6, v5, s[24:25]
	s_sub_u32 s14, s2, s3
	s_min_u32 s14, s14, 64
	s_mov_b32 s15, 0
	s_waitcnt vmcnt(0)
.Lagg_inner:
	s_sub_u32 s16, s14, s15
	s_min_u32 s16, s16, 8
	s_cmp_ge_u32 s16, 8
	s_cbranch_scc1 .Lagg_ld7
	s_cmp_ge_u32 s16, 7
	s_cbranch_scc1 .Lagg_ld6
	s_cmp_ge_u32 s16, 6
	s_cbranch_scc1 .Lagg_ld5
	s_cmp_ge_u32 s16, 5
	s_cbranch_scc1 .Lagg_ld4
	s_cmp_ge_u32 s16, 4
	s_cbranch_scc1 .Lagg_ld3
	s_cmp_ge_u32 s16, 3
	s_cbranch_scc1 .Lagg_ld2
	s_cmp_ge_u32 s16, 2
	s_cbranch_scc1 .Lagg_ld1
	s_branch .Lagg_ld0
.Lagg_ld7:
	s_add_u32 s17, s15, 7
	v_readlane_b32 s28, v6, s17
	s_mul_i32 s29, s28, 0x220
	s_add_u32 s54, s26, s29
	s_addc_u32 s55, s27, 0
	s_and_b32 s30, s28, 3
	s_lshl_b32 s30, s30, 4
	s_lshl_b64 s[30:31], 1, s30
	s_add_u32 s12, s12, s30
	s_addc_u32 s13, s13, s31
	global_load_dwordx2 v[62:63], v8, s[54:55]
	global_load_dword v39, v20, s[54:55] offset:512
.Lagg_ld6:
	s_add_u32 s17, s15, 6
	v_readlane_b32 s28, v6, s17
	s_mul_i32 s29, s28, 0x220
	s_add_u32 s52, s26, s29
	s_addc_u32 s53, s27, 0
	s_and_b32 s30, s28, 3
	s_lshl_b32 s30, s30, 4
	s_lshl_b64 s[30:31], 1, s30
	s_add_u32 s12, s12, s30
	s_addc_u32 s13, s13, s31
	global_load_dwordx2 v[60:61], v8, s[52:53]
	global_load_dword v38, v20, s[52:53] offset:512
.Lagg_ld5:
	s_add_u32 s17, s15, 5
	v_readlane_b32 s28, v6, s17
	s_mul_i32 s29, s28, 0x220
	s_add_u32 s50, s26, s29
	s_addc_u32 s51, s27, 0
	s_and_b32 s30, s28, 3
	s_lshl_b32 s30, s30, 4
	s_lshl_b64 s[30:31], 1, s30
	s_add_u32 s12, s12, s30
	s_addc_u32 s13, s13, s31
	global_load_dwordx2 v[58:59], v8, s[50:51]
	global_load_dword v37, v20, s[50:51] offset:512
.Lagg_ld4:
	s_add_u32 s17, s15, 4
	v_readlane_b32 s28, v6, s17
	s_mul_i32 s29, s28, 0x220
	s_add_u32 s48, s26, s29
	s_addc_u32 s49, s27, 0
	s_and_b32 s30, s28, 3
	s_lshl_b32 s30, s30, 4
	s_lshl_b64 s[30:31], 1, s30
	s_add_u32 s12, s12, s30
	s_addc_u32 s13, s13, s31
	global_load_dwordx2 v[56:57], v8, s[48:49]
	global_load_dword v36, v20, s[48:49] offset:512
.Lagg_ld3:
	s_add_u32 s17, s15, 3
	v_readlane_b32 s28, v6, s17
	s_mul_i32 s29, s28, 0x220
	s_add_u32 s46, s26, s29
	s_addc_u32 s47, s27, 0
	s_and_b32 s30, s28, 3
	s_lshl_b32 s30, s30, 4
	s_lshl_b64 s[30:31], 1, s30
	s_add_u32 s12, s12, s30
	s_addc_u32 s13, s13, s31
	global_load_dwordx2 v[54:55], v8, s[46:47]
	global_load_dword v35, v20, s[46:47] offset:512
.Lagg_ld2:
	s_add_u32 s17, s15, 2
	v_readlane_b32 s28, v6, s17
	s_mul_i32 s29, s28, 0x220
	s_add_u32 s44, s26, s29
	s_addc_u32 s45, s27, 0
	s_and_b32 s30, s28, 3
	s_lshl_b32 s30, s30, 4
	s_lshl_b64 s[30:31], 1, s30
	s_add_u32 s12, s12, s30
	s_addc_u32 s13, s13, s31
	global_load_dwordx2 v[52:53], v8, s[44:45]
	global_load_dword v34, v20, s[44:45] offset:512
.Lagg_ld1:
	s_add_u32 s17, s15, 1
	v_readlane_b32 s28, v6, s17
	s_mul_i32 s29, s28, 0x220
	s_add_u32 s42, s26, s29
	s_addc_u32 s43, s27, 0
	s_and_b32 s30, s28, 3
	s_lshl_b32 s30, s30, 4
	s_lshl_b64 s[30:31], 1, s30
	s_add_u32 s12, s12, s30
	s_addc_u32 s13, s13, s31
	global_load_dwordx2 v[50:51], v8, s[42:43]
	global_load_dword v33, v20, s[42:43] offset:512
.Lagg_ld0:
	s_add_u32 s17, s15, 0
	v_readlane_b32 s28, v6, s17
	s_mul_i32 s29, s28, 0x220
	s_add_u32 s40, s26, s29
	s_addc_u32 s41, s27, 0
	s_and_b32 s30, s28, 3
	s_lshl_b32 s30, s30, 4
	s_lshl_b64 s[30:31], 1, s30
	s_add_u32 s12, s12, s30
	s_addc_u32 s13, s13, s31
	global_load_dwordx2 v[48:49], v8, s[40:41]
	global_load_dword v32, v20, s[40:41] offset:512
	s_cmp_ge_u32 s16, 8
	s_cbranch_scc1 .Lagg_ac7
	s_cmp_ge_u32 s16, 7
	s_cbranch_scc1 .Lagg_ac6
	s_cmp_ge_u32 s16, 6
	s_cbranch_scc1 .Lagg_ac5
	s_cmp_ge_u32 s16, 5
	s_cbranch_scc1 .Lagg_ac4
	s_cmp_ge_u32 s16, 4
	s_cbranch_scc1 .Lagg_ac3
	s_cmp_ge_u32 s16, 3
	s_cbranch_scc1 .Lagg_ac2
	s_cmp_ge_u32 s16, 2
	s_cbranch_scc1 .Lagg_ac1
	s_branch .Lagg_ac0
.Lagg_ac7:
	s_waitcnt vmcnt(14)
	v_cvt_f32_i32_sdwa v40, sext(v62) dst_sel:DWORD dst_unused:UNUSED_PAD src0_sel:BYTE_0
	v_cvt_f32_i32_sdwa v41, sext(v62) dst_sel:DWORD dst_unused:UNUSED_PAD src0_sel:BYTE_1
	v_cvt_f32_i32_sdwa v42, sext(v62) dst_sel:DWORD dst_unused:UNUSED_PAD src0_sel:BYTE_2
	v_cvt_f32_i32_sdwa v43, sext(v62) dst_sel:DWORD dst_unused:UNUSED_PAD src0_sel:BYTE_3
	v_cvt_f32_i32_sdwa v44, sext(v63) dst_sel:DWORD dst_unused:UNUSED_PAD src0_sel:BYTE_0
	v_cvt_f32_i32_sdwa v45, sext(v63) dst_sel:DWORD dst_unused:UNUSED_PAD src0_sel:BYTE_1
	v_cvt_f32_i32_sdwa v46, sext(v63) dst_sel:DWORD dst_unused:UNUSED_PAD src0_sel:BYTE_2
	v_cvt_f32_i32_sdwa v47, sext(v63) dst_sel:DWORD dst_unused:UNUSED_PAD src0_sel:BYTE_3
	v_pk_fma_f32 v[16:17], v[38:39], v[40:41], v[16:17] op_sel:[1,0,0] op_sel_hi:[1,1,1]
	v_pk_fma_f32 v[14:15], v[38:39], v[42:43], v[14:15] op_sel:[1,0,0] op_sel_hi:[1,1,1]
	v_pk_fma_f32 v[12:13], v[38:39], v[44:45], v[12:13] op_sel:[1,0,0] op_sel_hi:[1,1,1]
	v_pk_fma_f32 v[10:11], v[38:39], v[46:47], v[10:11] op_sel:[1,0,0] op_sel_hi:[1,1,1]
.Lagg_ac6:
	s_waitcnt vmcnt(12)
	v_cvt_f32_i32_sdwa v40, sext(v60) dst_sel:DWORD dst_unused:UNUSED_PAD src0_sel:BYTE_0
	v_cvt_f32_i32_sdwa v41, sext(v60) dst_sel:DWORD dst_unused:UNUSED_PAD src0_sel:BYTE_1
	v_cvt_f32_i32_sdwa v42, sext(v60) dst_sel:DWORD dst_unused:UNUSED_PAD src0_sel:BYTE_2
	v_cvt_f32_i32_sdwa v43, sext(v60) dst_sel:DWORD dst_unused:UNUSED_PAD src0_sel:BYTE_3
	v_cvt_f32_i32_sdwa v44, sext(v61) dst_sel:DWORD dst_unused:UNUSED_PAD src0_sel:BYTE_0
	v_cvt_f32_i32_sdwa v45, sext(v61) dst_sel:DWORD dst_unused:UNUSED_PAD src0_sel:BYTE_1
	v_cvt_f32_i32_sdwa v46, sext(v61) dst_sel:DWORD dst_unused:UNUSED_PAD src0_sel:BYTE_2
	v_cvt_f32_i32_sdwa v47, sext(v61) dst_sel:DWORD dst_unused:UNUSED_PAD src0_sel:BYTE_3
	v_pk_fma_f32 v[16:17], v[38:39], v[40:41], v[16:17] op_sel_hi:[0,1,1]
	v_pk_fma_f32 v[14:15], v[38:39], v[42:43], v[14:15] op_sel_hi:[0,1,1]
	v_pk_fma_f32 v[12:13], v[38:39], v[44:45], v[12:13] op_sel_hi:[0,1,1]
	v_pk_fma_f32 v[10:11], v[38:39], v[46:47], v[10:11] op_sel_hi:[0,1,1]
.Lagg_ac5:
	s_waitcnt vmcnt(10)
	v_cvt_f32_i32_sdwa v40, sext(v58) dst_sel:DWORD dst_unused:UNUSED_PAD src0_sel:BYTE_0
	v_cvt_f32_i32_sdwa v41, sext(v58) dst_sel:DWORD dst_unused:UNUSED_PAD src0_sel:BYTE_1
	v_cvt_f32_i32_sdwa v42, sext(v58) dst_sel:DWORD dst_unused:UNUSED_PAD src0_sel:BYTE_2
	v_cvt_f32_i32_sdwa v43, sext(v58) dst_sel:DWORD dst_unused:UNUSED_PAD src0_sel:BYTE_3
	v_cvt_f32_i32_sdwa v44, sext(v59) dst_sel:DWORD dst_unused:UNUSED_PAD src0_sel:BYTE_0
	v_cvt_f32_i32_sdwa v45, sext(v59) dst_sel:DWORD dst_unused:UNUSED_PAD src0_sel:BYTE_1
	v_cvt_f32_i32_sdwa v46, sext(v59) dst_sel:DWORD dst_unused:UNUSED_PAD src0_sel:BYTE_2
	v_cvt_f32_i32_sdwa v47, sext(v59) dst_sel:DWORD dst_unused:UNUSED_PAD src0_sel:BYTE_3
	v_pk_fma_f32 v[16:17], v[36:37], v[40:41], v[16:17] op_sel:[1,0,0] op_sel_hi:[1,1,1]
	v_pk_fma_f32 v[14:15], v[36:37], v[42:43], v[14:15] op_sel:[1,0,0] op_sel_hi:[1,1,1]
	v_pk_fma_f32 v[12:13], v[36:37], v[44:45], v[12:13] op_sel:[1,0,0] op_sel_hi:[1,1,1]
	v_pk_fma_f32 v[10:11], v[36:37], v[46:47], v[10:11] op_sel:[1,0,0] op_sel_hi:[1,1,1]
.Lagg_ac4:
	s_waitcnt vmcnt(8)
	v_cvt_f32_i32_sdwa v40, sext(v56) dst_sel:DWORD dst_unused:UNUSED_PAD src0_sel:BYTE_0
	v_cvt_f32_i32_sdwa v41, sext(v56) dst_sel:DWORD dst_unused:UNUSED_PAD src0_sel:BYTE_1
	v_cvt_f32_i32_sdwa v42, sext(v56) dst_sel:DWORD dst_unused:UNUSED_PAD src0_sel:BYTE_2
	v_cvt_f32_i32_sdwa v43, sext(v56) dst_sel:DWORD dst_unused:UNUSED_PAD src0_sel:BYTE_3
	v_cvt_f32_i32_sdwa v44, sext(v57) dst_sel:DWORD dst_unused:UNUSED_PAD src0_sel:BYTE_0
	v_cvt_f32_i32_sdwa v45, sext(v57) dst_sel:DWORD dst_unused:UNUSED_PAD src0_sel:BYTE_1
	v_cvt_f32_i32_sdwa v46, sext(v57) dst_sel:DWORD dst_unused:UNUSED_PAD src0_sel:BYTE_2
	v_cvt_f32_i32_sdwa v47, sext(v57) dst_sel:DWORD dst_unused:UNUSED_PAD src0_sel:BYTE_3
	v_pk_fma_f32 v[16:17], v[36:37], v[40:41], v[16:17] op_sel_hi:[0,1,1]
	v_pk_fma_f32 v[14:15], v[36:37], v[42:43], v[14:15] op_sel_hi:[0,1,1]
	v_pk_fma_f32 v[12:13], v[36:37], v[44:45], v[12:13] op_sel_hi:[0,1,1]
	v_pk_fma_f32 v[10:11], v[36:37], v[46:47], v[10:11] op_sel_hi:[0,1,1]
.Lagg_ac3:
	s_waitcnt vmcnt(6)
	v_cvt_f32_i32_sdwa v40, sext(v54) dst_sel:DWORD dst_unused:UNUSED_PAD src0_sel:BYTE_0
	v_cvt_f32_i32_sdwa v41, sext(v54) dst_sel:DWORD dst_unused:UNUSED_PAD src0_sel:BYTE_1
	v_cvt_f32_i32_sdwa v42, sext(v54) dst_sel:DWORD dst_unused:UNUSED_PAD src0_sel:BYTE_2
	v_cvt_f32_i32_sdwa v43, sext(v54) dst_sel:DWORD dst_unused:UNUSED_PAD src0_sel:BYTE_3
	v_cvt_f32_i32_sdwa v44, sext(v55) dst_sel:DWORD dst_unused:UNUSED_PAD src0_sel:BYTE_0
	v_cvt_f32_i32_sdwa v45, sext(v55) dst_sel:DWORD dst_unused:UNUSED_PAD src0_sel:BYTE_1
	v_cvt_f32_i32_sdwa v46, sext(v55) dst_sel:DWORD dst_unused:UNUSED_PAD src0_sel:BYTE_2
	v_cvt_f32_i32_sdwa v47, sext(v55) dst_sel:DWORD dst_unused:UNUSED_PAD src0_sel:BYTE_3
	v_pk_fma_f32 v[16:17], v[34:35], v[40:41], v[16:17] op_sel:[1,0,0] op_sel_hi:[1,1,1]
	v_pk_fma_f32 v[14:15], v[34:35], v[42:43], v[14:15] op_sel:[1,0,0] op_sel_hi:[1,1,1]
	v_pk_fma_f32 v[12:13], v[34:35], v[44:45], v[12:13] op_sel:[1,0,0] op_sel_hi:[1,1,1]
	v_pk_fma_f32 v[10:11], v[34:35], v[46:47], v[10:11] op_sel:[1,0,0] op_sel_hi:[1,1,1]
.Lagg_ac2:
	s_waitcnt vmcnt(4)
	v_cvt_f32_i32_sdwa v40, sext(v52) dst_sel:DWORD dst_unused:UNUSED_PAD src0_sel:BYTE_0
	v_cvt_f32_i32_sdwa v41, sext(v52) dst_sel:DWORD dst_unused:UNUSED_PAD src0_sel:BYTE_1
	v_cvt_f32_i32_sdwa v42, sext(v52) dst_sel:DWORD dst_unused:UNUSED_PAD src0_sel:BYTE_2
	v_cvt_f32_i32_sdwa v43, sext(v52) dst_sel:DWORD dst_unused:UNUSED_PAD src0_sel:BYTE_3
	v_cvt_f32_i32_sdwa v44, sext(v53) dst_sel:DWORD dst_unused:UNUSED_PAD src0_sel:BYTE_0
	v_cvt_f32_i32_sdwa v45, sext(v53) dst_sel:DWORD dst_unused:UNUSED_PAD src0_sel:BYTE_1
	v_cvt_f32_i32_sdwa v46, sext(v53) dst_sel:DWORD dst_unused:UNUSED_PAD src0_sel:BYTE_2
	v_cvt_f32_i32_sdwa v47, sext(v53) dst_sel:DWORD dst_unused:UNUSED_PAD src0_sel:BYTE_3
	v_pk_fma_f32 v[16:17], v[34:35], v[40:41], v[16:17] op_sel_hi:[0,1,1]
	v_pk_fma_f32 v[14:15], v[34:35], v[42:43], v[14:15] op_sel_hi:[0,1,1]
	v_pk_fma_f32 v[12:13], v[34:35], v[44:45], v[12:13] op_sel_hi:[0,1,1]
	v_pk_fma_f32 v[10:11], v[34:35], v[46:47], v[10:11] op_sel_hi:[0,1,1]
.Lagg_ac1:
	s_waitcnt vmcnt(2)
	v_cvt_f32_i32_sdwa v40, sext(v50) dst_sel:DWORD dst_unused:UNUSED_PAD src0_sel:BYTE_0
	v_cvt_f32_i32_sdwa v41, sext(v50) dst_sel:DWORD dst_unused:UNUSED_PAD src0_sel:BYTE_1
	v_cvt_f32_i32_sdwa v42, sext(v50) dst_sel:DWORD dst_unused:UNUSED_PAD src0_sel:BYTE_2
	v_cvt_f32_i32_sdwa v43, sext(v50) dst_sel:DWORD dst_unused:UNUSED_PAD src0_sel:BYTE_3
	v_cvt_f32_i32_sdwa v44, sext(v51) dst_sel:DWORD dst_unused:UNUSED_PAD src0_sel:BYTE_0
	v_cvt_f32_i32_sdwa v45, sext(v51) dst_sel:DWORD dst_unused:UNUSED_PAD src0_sel:BYTE_1
	v_cvt_f32_i32_sdwa v46, sext(v51) dst_sel:DWORD dst_unused:UNUSED_PAD src0_sel:BYTE_2
	v_cvt_f32_i32_sdwa v47, sext(v51) dst_sel:DWORD dst_unused:UNUSED_PAD src0_sel:BYTE_3
	v_pk_fma_f32 v[16:17], v[32:33], v[40:41], v[16:17] op_sel:[1,0,0] op_sel_hi:[1,1,1]
	v_pk_fma_f32 v[14:15], v[32:33], v[42:43], v[14:15] op_sel:[1,0,0] op_sel_hi:[1,1,1]
	v_pk_fma_f32 v[12:13], v[32:33], v[44:45], v[12:13] op_sel:[1,0,0] op_sel_hi:[1,1,1]
	v_pk_fma_f32 v[10:11], v[32:33], v[46:47], v[10:11] op_sel:[1,0,0] op_sel_hi:[1,1,1]
.Lagg_ac0:
	s_waitcnt vmcnt(0)
	v_cvt_f32_i32_sdwa v40, sext(v48) dst_sel:DWORD dst_unused:UNUSED_PAD src0_sel:BYTE_0
	v_cvt_f32_i32_sdwa v41, sext(v48) dst_sel:DWORD dst_unused:UNUSED_PAD src0_sel:BYTE_1
	v_cvt_f32_i32_sdwa v42, sext(v48) dst_sel:DWORD dst_unused:UNUSED_PAD src0_sel:BYTE_2
	v_cvt_f32_i32_sdwa v43, sext(v48) dst_sel:DWORD dst_unused:UNUSED_PAD src0_sel:BYTE_3
	v_cvt_f32_i32_sdwa v44, sext(v49) dst_sel:DWORD dst_unused:UNUSED_PAD src0_sel:BYTE_0
	v_cvt_f32_i32_sdwa v45, sext(v49) dst_sel:DWORD dst_unused:UNUSED_PAD src0_sel:BYTE_1
	v_cvt_f32_i32_sdwa v46, sext(v49) dst_sel:DWORD dst_unused:UNUSED_PAD src0_sel:BYTE_2
	v_cvt_f32_i32_sdwa v47, sext(v49) dst_sel:DWORD dst_unused:UNUSED_PAD src0_sel:BYTE_3
	v_pk_fma_f32 v[16:17], v[32:33], v[40:41], v[16:17] op_sel_hi:[0,1,1]
	v_pk_fma_f32 v[14:15], v[32:33], v[42:43], v[14:15] op_sel_hi:[0,1,1]
	v_pk_fma_f32 v[12:13], v[32:33], v[44:45], v[12:13] op_sel_hi:[0,1,1]
	v_pk_fma_f32 v[10:11], v[32:33], v[46:47], v[10:11] op_sel_hi:[0,1,1]
	s_add_u32 s15, s15, 8
	s_cmp_lt_u32 s15, s14
	s_cbranch_scc1 .Lagg_inner
	s_add_u32 s3, s3, 64
	s_cmp_lt_u32 s3, s2
	s_cbranch_scc1 .Lagg_outer
	v_mov_b32_e32 v18, s12
	v_mov_b32_e32 v19, s13

	.amdhsa_kernel _Z7agg_ln1PKDF16_S0_S0_PKiS2_S2_PKfS4_S4_PDF16_S4_S4_S5_S5_
		.amdhsa_group_segment_fixed_size 16640
		.amdhsa_private_segment_fixed_size 0
		.amdhsa_kernarg_size 112
		.amdhsa_user_sgpr_count 2
		.amdhsa_user_sgpr_dispatch_ptr 0
		.amdhsa_user_sgpr_queue_ptr 0
		.amdhsa_user_sgpr_kernarg_segment_ptr 1
		.amdhsa_user_sgpr_dispatch_id 0
		.amdhsa_user_sgpr_kernarg_preload_length 0
		.amdhsa_user_sgpr_kernarg_preload_offset 0
		.amdhsa_user_sgpr_private_segment_size 0
		.amdhsa_uses_dynamic_stack 0
		.amdhsa_enable_private_segment 0
		.amdhsa_system_sgpr_workgroup_id_x 1
		.amdhsa_system_sgpr_workgroup_id_y 0
		.amdhsa_system_sgpr_workgroup_id_z 0
		.amdhsa_system_sgpr_workgroup_info 0
		.amdhsa_system_vgpr_workitem_id 0
		.amdhsa_next_free_vgpr 64
		.amdhsa_next_free_sgpr 64
		.amdhsa_accum_offset 64
		.amdhsa_reserve_vcc 1
		.amdhsa_float_round_mode_32 0
		.amdhsa_float_round_mode_16_64 0
		.amdhsa_float_denorm_mode_32 3
		.amdhsa_float_denorm_mode_16_64 3
		.amdhsa_dx10_clamp 1
		.amdhsa_ieee_mode 1
		.amdhsa_fp16_overflow 0
		.amdhsa_tg_split 0
		.amdhsa_exception_fp_ieee_invalid_op 0
		.amdhsa_exception_fp_denorm_src 0
		.amdhsa_exception_fp_ieee_div_zero 0
		.amdhsa_exception_fp_ieee_overflow 0
		.amdhsa_exception_fp_ieee_underflow 0
		.amdhsa_exception_fp_ieee_inexact 0
		.amdhsa_exception_int_div_zero 0
	.end_amdhsa_kernel

_Z5ln2_kPKDF16_PKfS2_Pf:
	v_lshl_or_b32 v1, s2, 8, v0
	s_mov_b32 s2, 0x9c400
	v_cmp_gt_u32_e32 vcc, s2, v1
	s_and_saveexec_b64 s[2:3], vcc
	s_cbranch_execz .LBB2_2
	s_load_dwordx8 s[4:11], s[0:1], 0x0
	v_lshlrev_b32_e32 v0, 3, v0
	v_lshlrev_b32_e32 v1, 3, v1
	v_and_b32_e32 v4, 0x1f8, v0
	s_mov_b32 s0, 0x7ffe00
	v_and_or_b32 v32, v1, s0, v4
	v_lshlrev_b32_e32 v0, 1, v32
	s_waitcnt lgkmcnt(0)
	global_load_dwordx4 v[0:3], v0, s[4:5] nt
	v_lshlrev_b32_e32 v20, 2, v4
	global_load_dwordx4 v[4:7], v20, s[6:7]
	global_load_dwordx4 v[8:11], v20, s[8:9]
	global_load_dwordx4 v[12:15], v20, s[6:7] offset:16
	global_load_dwordx4 v[16:19], v20, s[8:9] offset:16
	v_mov_b32_e32 v24, 0
	v_mov_b32_e32 v25, 0
	v_mov_b32_e32 v34, 0x3b000000
	v_mov_b32_e32 v35, 0
	v_mov_b32_e32 v33, 0
	v_mov_b32_e32 v36, 0x3727c5ac
	s_mov_b32 s0, 0x800000
	s_waitcnt vmcnt(4)
	v_cvt_f32_f16_e32 v20, v0
	v_cvt_f32_f16_sdwa v21, v0 dst_sel:DWORD dst_unused:UNUSED_PAD src0_sel:WORD_1
	v_cvt_f32_f16_e32 v0, v1
	v_cvt_f32_f16_sdwa v1, v1 dst_sel:DWORD dst_unused:UNUSED_PAD src0_sel:WORD_1
	v_cvt_f32_f16_e32 v22, v2
	v_add_f32_e32 v26, 0, v20
	v_cvt_f32_f16_sdwa v23, v2 dst_sel:DWORD dst_unused:UNUSED_PAD src0_sel:WORD_1
	v_add_f32_e32 v26, v26, v21
	v_cvt_f32_f16_e32 v2, v3
	v_add_f32_e32 v26, v26, v0
	v_cvt_f32_f16_sdwa v3, v3 dst_sel:DWORD dst_unused:UNUSED_PAD src0_sel:WORD_1
	v_add_f32_e32 v26, v26, v1
	v_add_f32_e32 v26, v26, v22
	v_add_f32_e32 v26, v26, v23
	v_add_f32_e32 v26, v26, v2
	v_add_f32_e32 v26, v26, v3
	s_nop 1
	v_add_f32_dpp v26, v26, v26 quad_perm:[1,0,3,2] row_mask:0xf bank_mask:0xf bound_ctrl:1
	s_nop 1
	v_add_f32_dpp v26, v26, v26 quad_perm:[2,3,0,1] row_mask:0xf bank_mask:0xf bound_ctrl:1
	s_nop 1
	v_add_f32_dpp v26, v26, v26 row_half_mirror row_mask:0xf bank_mask:0xf bound_ctrl:1
	s_nop 1
	v_add_f32_dpp v26, v26, v26 row_mirror row_mask:0xf bank_mask:0xf bound_ctrl:1
	s_nop 1
	v_mov_b32_dpp v24, v26 row_bcast:15 row_mask:0xa bank_mask:0xf
	v_add_f32_e32 v24, v26, v24
	s_nop 1
	v_mov_b32_dpp v25, v24 row_bcast:31 row_mask:0xc bank_mask:0xf
	v_add_f32_e32 v24, v24, v25
	s_nop 0
	v_readlane_b32 s1, v24, 63
	s_nop 1
	v_mul_f32_e32 v24, s1, v34
	v_pk_add_f32 v[20:21], v[20:21], v[24:25] op_sel_hi:[1,0] neg_lo:[0,1] neg_hi:[0,1]
	v_pk_add_f32 v[0:1], v[0:1], v[24:25] op_sel_hi:[1,0] neg_lo:[0,1] neg_hi:[0,1]
	v_pk_add_f32 v[22:23], v[22:23], v[24:25] op_sel_hi:[1,0] neg_lo:[0,1] neg_hi:[0,1]
	v_pk_add_f32 v[2:3], v[2:3], v[24:25] op_sel_hi:[1,0] neg_lo:[0,1] neg_hi:[0,1]
	v_pk_mul_f32 v[24:25], v[20:21], v[20:21]
	v_pk_mul_f32 v[26:27], v[0:1], v[0:1]
	v_add_f32_e32 v24, v24, v25
	v_add_f32_e32 v24, v24, v26
	v_pk_mul_f32 v[28:29], v[22:23], v[22:23]
	v_add_f32_e32 v24, v24, v27
	v_add_f32_e32 v24, v24, v28
	v_pk_mul_f32 v[30:31], v[2:3], v[2:3]
	v_add_f32_e32 v24, v24, v29
	v_add_f32_e32 v24, v24, v30
	v_add_f32_e32 v24, v24, v31
	v_lshlrev_b32_e32 v28, 2, v32
	s_nop 0
	v_add_f32_dpp v24, v24, v24 quad_perm:[1,0,3,2] row_mask:0xf bank_mask:0xf bound_ctrl:1
	s_nop 1
	v_add_f32_dpp v24, v24, v24 quad_perm:[2,3,0,1] row_mask:0xf bank_mask:0xf bound_ctrl:1
	s_nop 1
	v_add_f32_dpp v24, v24, v24 row_half_mirror row_mask:0xf bank_mask:0xf bound_ctrl:1
	s_nop 1
	v_add_f32_dpp v24, v24, v24 row_mirror row_mask:0xf bank_mask:0xf bound_ctrl:1
	s_nop 1
	v_mov_b32_dpp v35, v24 row_bcast:15 row_mask:0xa bank_mask:0xf
	v_add_f32_e32 v24, v24, v35
	s_nop 1
	v_mov_b32_dpp v33, v24 row_bcast:31 row_mask:0xc bank_mask:0xf
	v_add_f32_e32 v24, v24, v33
	s_nop 0
	v_readlane_b32 s1, v24, 63
	s_nop 1
	v_fmac_f32_e32 v36, s1, v34
	v_mul_f32_e32 v24, 0x4b800000, v36
	v_cmp_gt_f32_e32 vcc, s0, v36
	s_nop 1
	v_cndmask_b32_e32 v24, v36, v24, vcc
	v_rsq_f32_e32 v24, v24
	s_nop 0
	v_mul_f32_e32 v25, 0x45800000, v24
	v_cndmask_b32_e32 v24, v24, v25, vcc
	v_pk_mul_f32 v[20:21], v[20:21], v[24:25] op_sel_hi:[1,0]
	v_pk_mul_f32 v[26:27], v[0:1], v[24:25] op_sel_hi:[1,0]
	v_pk_mul_f32 v[22:23], v[22:23], v[24:25] op_sel_hi:[1,0]
	v_pk_mul_f32 v[24:25], v[2:3], v[24:25] op_sel_hi:[1,0]
	s_waitcnt vmcnt(2)
	v_pk_fma_f32 v[0:1], v[4:5], v[20:21], v[8:9]
	v_pk_fma_f32 v[2:3], v[6:7], v[26:27], v[10:11]
	s_waitcnt vmcnt(0)
	v_pk_fma_f32 v[4:5], v[12:13], v[22:23], v[16:17]
	v_pk_fma_f32 v[6:7], v[14:15], v[24:25], v[18:19]
	global_store_dwordx4 v28, v[0:3], s[10:11] nt
	global_store_dwordx4 v28, v[4:7], s[10:11] offset:16 nt
